# v8 + 28 of 128 expert weight mats converted to fp8 in the idle att-half of the ut_att phases instead of the prologue (P=100,Q=114)
# speedup vs baseline: 1.0021x; 1.0021x over previous
.LBB0_654:
	s_barrier
	v_readlane_b32 s46, v255, 4
	s_sub_i32 s42, s88, 0x80
	s_lshl_b32 s42, s42, 3
	s_lshr_b32 s5, s33, 6
	s_add_i32 s42, s42, s5
	s_mul_i32 s5, s5, 0x4200
	s_movk_i32 s45, 114
	s_movk_i32 s4, 14
	s_movk_i32 vcc_lo, 100
	s_movk_i32 vcc_hi, 14
	s_cmp_eq_u32 s46, 1
	s_cselect_b32 s45, vcc_lo, s45
	s_cselect_b32 s4, vcc_hi, s4
	s_lshl_b32 s44, s4, 9
	s_mul_i32 s43, s4, 0x300
	v_readlane_b32 s8, v252, 0
	v_readlane_b32 s9, v252, 1
	v_mbcnt_lo_u32_b32 v13, -1, 0
	v_mbcnt_hi_u32_b32 v13, -1, v13
	s_load_dwordx2 s[6:7], s[8:9], 0xa0
	s_load_dwordx2 s[10:11], s[8:9], 0xd8
	s_load_dwordx2 s[8:9], s[8:9], 0xb0
	s_movk_i32 s46, 0x84
	s_movk_i32 s47, 0x840
	v_and_b32_e32 v14, 31, v13
	v_lshlrev_b32_e32 v14, 2, v14
	v_lshrrev_b32_e32 v15, 5, v13
	v_mov_b32_e32 v4, s5
	v_mad_u32_u24 v4, v15, s46, v4
	v_add_u32_e32 v4, v4, v14
	v_and_b32_e32 v10, 7, v13
	v_lshrrev_b32_e32 v11, 3, v13
	v_mov_b32_e32 v5, s5
	v_mad_u32_u24 v5, v10, s47, v5
	v_lshl_add_u32 v5, v11, 2, v5
	v_lshlrev_b32_e32 v6, 10, v11
	v_lshl_add_u32 v6, v10, 4, v6
	v_add_u32_e32 v7, 0x2000, v6
	v_add_u32_e32 v8, 0x4000, v6
	v_add_u32_e32 v9, 0x6000, v6
	s_waitcnt lgkmcnt(0)
	s_cmp_lt_u32 s42, s43
	s_cbranch_scc0 .Lcv_done
	s_cmp_lt_u32 s42, s44
	s_cbranch_scc0 .Lcv_dn0
	s_lshr_b32 s4, s42, 9
	s_add_i32 s4, s4, s45
	s_bfe_u32 s5, s42, 0x30006
	s_and_b32 vcc_lo, s42, 63
	s_lshl_b32 s46, s4, 23
	s_lshl_b32 s47, s5, 20
	s_add_u32 s46, s46, s47
	s_lshl_b32 s47, vcc_lo, 7
	s_add_u32 s46, s46, s47
	s_add_u32 s46, s46, s6
	s_addc_u32 s47, s7, 0
	s_lshl_b32 s52, s4, 21
	s_add_u32 s52, s52, 0x4400000
	s_lshl_b32 s53, s5, 7
	s_add_u32 s52, s52, s53
	s_bfe_u32 s53, vcc_lo, 0x30002
	s_lshl_b32 s53, s53, 18
	s_add_u32 s52, s52, s53
	s_lshr_b32 s53, vcc_lo, 5
	s_lshl_b32 s53, s53, 17
	s_add_u32 s52, s52, s53
	s_and_b32 s53, vcc_lo, 3
	s_lshl_b32 s53, s53, 15
	s_add_u32 s52, s52, s53
	s_add_u32 s52, s52, s10
	s_addc_u32 s53, s11, 0
	s_mov_b32 s51, 0x42000000
	s_movk_i32 s5, 0x2000
	s_movk_i32 s4, 0x4000
	s_branch .Lcv_ld0

c_jobs:
	.long	4
	.long	2840
	.long	1024
	.long	0
	.long	1024
	.long	0
	.long	1
	.long	2
	.quad	2908160
	.quad	2097152
	.quad	2097152
	.long	0
	.long	0
	.long	4
	.long	2840
	.long	1024
	.long	1536
	.long	512
	.long	1024
	.long	1
	.long	2
	.quad	2908160
	.quad	2097152
	.quad	2097152
	.long	0
	.long	0
	.long	4
	.long	2840
	.long	1024
	.long	2048
	.long	128
	.long	1536
	.long	1
	.long	2
	.quad	2908160
	.quad	2097152
	.quad	2097152
	.long	0
	.long	0
	.long	4
	.long	2840
	.long	1024
	.long	2176
	.long	128
	.long	1664
	.long	1
	.long	2
	.quad	2908160
	.quad	2097152
	.quad	2097152
	.long	0
	.long	0
	.long	4
	.long	2840
	.long	1024
	.long	2304
	.long	128
	.long	1792
	.long	1
	.long	2
	.quad	2908160
	.quad	2097152
	.quad	2097152
	.long	0
	.long	0
	.long	4
	.long	2840
	.long	1024
	.long	2560
	.long	128
	.long	1920
	.long	1
	.long	2
	.quad	2908160
	.quad	2097152
	.quad	2097152
	.long	0
	.long	0
	.long	4
	.long	2840
	.long	1024
	.long	1024
	.long	512
	.long	0
	.long	0
	.long	2
	.quad	2908160
	.quad	10485760
	.quad	786432
	.long	0
	.long	0
	.long	4
	.long	2840
	.long	1024
	.long	2432
	.long	128
	.long	512
	.long	0
	.long	2
	.quad	2908160
	.quad	10485760
	.quad	786432
	.long	0
	.long	0
	.long	4
	.long	2840
	.long	1024
	.long	2688
	.long	128
	.long	640
	.long	0
	.long	2
	.quad	2908160
	.quad	10485760
	.quad	786432
	.long	0
	.long	0
	.long	5
	.long	1024
	.long	1024
	.long	0
	.long	1024
	.long	0
	.long	0
	.long	2
	.quad	1048576
	.quad	13631488
	.quad	1048576
	.long	64
	.long	0
	.long	13
	.long	256
	.long	2048
	.long	0
	.long	256
	.long	0
	.long	0
	.long	4
	.quad	524288
	.quad	17825792
	.quad	524288
	.long	0
	.long	0
	.long	15
	.long	6144
	.long	1024
	.long	0
	.long	2048
	.long	0
	.long	0
	.long	2
	.quad	6291456
	.quad	22020096
	.quad	4194304
	.long	32
	.long	0
	.long	15
	.long	6144
	.long	1024
	.long	4096
	.long	2048
	.long	2048
	.long	0
	.long	2
	.quad	6291456
	.quad	22020096
	.quad	4194304
	.long	32
	.long	0
	.long	15
	.long	6144
	.long	1024
	.long	2048
	.long	2048
	.long	0
	.long	0
	.long	2
	.quad	6291456
	.quad	38797312
	.quad	2097152
	.long	32
	.long	0
	.long	16
	.long	1024
	.long	2048
	.long	0
	.long	1024
	.long	0
	.long	0
	.long	2
	.quad	2097152
	.quad	51380224
	.quad	2097152
	.long	128
	.long	0
	.long	20
	.long	2048
	.long	1024
	.long	0
	.long	2048
	.long	0
	.long	2
	.long	100
	.quad	2097152
	.quad	71303168
	.quad	2097152
	.long	32
	.long	0
	.long	22
	.long	1024
	.long	1024
	.long	0
	.long	1024
	.long	0
	.long	0
	.long	100
	.quad	1048576
	.quad	608174080
	.quad	1048576
	.long	64
	.long	0
	.long	24
	.long	1024
	.long	256
	.long	0
	.long	1024
	.long	0
	.long	0
	.long	4
	.quad	262144
	.quad	59768832
	.quad	262144
	.long	0
	.long	0
	.long	25
	.long	1024
	.long	1024
	.long	0
	.long	1024
	.long	0
	.long	0
	.long	4
	.quad	1048576
	.quad	61865984
	.quad	1048576
	.long	32
	.long	0
	.size	c_jobs, 1216

	.type	__hip_cuid_b50e1a6430de2f85,@object
